# proj gemm: residual tile loads moved from prologue into first K-loop iteration with counted vmcnt
# speedup vs baseline: 1.0006x; 1.0006x over previous
.LBB3_38:
	s_endpgm
	.p2align	8

.LBB4_6:
	v_lshlrev_b32_e32 v1, 4, v0
	v_and_b32_e32 v2, 32, v0
	v_bitop3_b32 v1, v1, v2, 48 bitop3:0x6c
	v_lshrrev_b32_e32 v3, 3, v0
	v_bfe_u32 v62, v0, 2, 4
	v_lshrrev_b32_e32 v50, 1, v1
	v_and_b32_e32 v1, 48, v3
	v_lshrrev_b32_e32 v2, 1, v0
	v_or_b32_e32 v4, v1, v62
	v_and_b32_e32 v51, 32, v2
	v_mul_lo_u32 v5, s7, v4
	v_or_b32_e32 v2, v51, v50
	v_add_lshl_u32 v110, v5, v2, 1
	s_waitcnt lgkmcnt(0)
	v_mad_u64_u32 v[4:5], s[20:21], s30, v4, v[2:3]
	s_movk_i32 s20, 0x70
	s_nop 0
	v_bitop3_b32 v64, v3, s20, 64 bitop3:0xc8
	v_or_b32_e32 v3, v64, v62
	s_lshl_b32 s42, s22, 3
	v_mul_lo_u32 v5, s7, v3
	v_mul_lo_u32 v3, s30, v3
	s_abs_i32 s43, s42
	v_add_lshl_u32 v114, v5, v2, 1
	v_add_lshl_u32 v116, v3, v2, 1
	v_cvt_f32_u32_e32 v2, s43
	s_lshr_b32 s27, s33, 6
	s_lshl_b32 s44, s27, 10
	s_sub_i32 s27, 0, s43
	v_rcp_iflag_f32_e32 v2, v2
	s_add_i32 s23, s23, s26
	s_ashr_i32 s26, s23, 31
	s_bfe_i32 s45, s22, 0x1001c
	v_mul_f32_e32 v2, 0x4f7ffffe, v2
	v_cvt_u32_f32_e32 v2, v2
	s_xor_b32 s22, s26, s45
	s_abs_i32 s26, s23
	s_lshl_b32 s20, s30, 7
	v_readfirstlane_b32 s46, v2
	s_mul_i32 s27, s27, s46
	s_mul_hi_u32 s27, s46, s27
	s_add_i32 s46, s46, s27
	s_mul_hi_u32 s27, s26, s46
	s_mul_i32 s34, s27, s43
	s_lshr_b32 s25, s33, 8
	s_ashr_i32 s29, s7, 31
	s_mov_b32 s28, s7
	s_sub_i32 s26, s26, s34
	s_bfe_u32 s24, s33, 0x20006
	v_add_lshl_u32 v118, v4, s20, 1
	s_lshl_b64 s[20:21], s[28:29], 8
	s_lshl_b32 s31, s25, 6
	s_add_i32 s34, s27, 1
	s_sub_i32 s35, s26, s43
	s_cmp_ge_u32 s26, s43
	s_cselect_b32 s27, s34, s27
	s_cselect_b32 s26, s35, s26
	s_add_i32 s34, s27, 1
	s_cmp_ge_u32 s26, s43
	s_cselect_b32 s26, s34, s27
	s_xor_b32 s26, s26, s22
	s_sub_i32 s22, s26, s22
	s_lshl_b32 s26, s22, 3
	s_sub_i32 s27, s3, s26
	s_min_i32 s27, s27, 8
	s_abs_i32 s35, s27
	v_cvt_f32_u32_e32 v2, s35
	s_sub_i32 s50, 0, s35
	s_mul_i32 s22, s22, s42
	s_sub_i32 s22, s23, s22
	v_rcp_iflag_f32_e32 v2, v2
	s_abs_i32 s49, s22
	s_xor_b32 s23, s22, s27
	s_ashr_i32 s23, s23, 31
	v_mul_f32_e32 v2, 0x4f7ffffe, v2
	v_cvt_u32_f32_e32 v2, v2
	s_mul_i32 s48, s30, 0x180
	s_mul_hi_i32 s47, s30, 0x180
	v_and_b32_e32 v65, 15, v0
	v_readfirstlane_b32 s51, v2
	s_mul_i32 s50, s50, s51
	s_mul_hi_u32 s50, s51, s50
	s_add_i32 s51, s51, s50
	s_mul_hi_u32 s50, s49, s51
	s_mul_i32 s51, s50, s35
	s_sub_i32 s49, s49, s51
	s_add_i32 s51, s50, 1
	s_sub_i32 s52, s49, s35
	s_cmp_ge_u32 s49, s35
	s_cselect_b32 s50, s51, s50
	s_cselect_b32 s49, s52, s49
	s_add_i32 s51, s50, 1
	s_cmp_ge_u32 s49, s35
	s_cselect_b32 s35, s51, s50
	s_xor_b32 s35, s35, s23
	s_sub_i32 s66, s35, s23
	s_mul_i32 s23, s66, s27
	s_sub_i32 s22, s22, s23
	s_add_i32 s65, s22, s26
	s_ashr_i32 s22, s65, 31
	s_mul_i32 s22, s20, s22
	s_mul_hi_u32 s23, s20, s65
	s_add_i32 s26, s23, s22
	s_lshr_b64 s[22:23], s[28:29], 24
	s_mul_i32 s22, s22, s65
	s_add_i32 s22, s26, s22
	s_mul_i32 s23, s20, s65
	s_add_u32 s26, s16, s23
	s_addc_u32 s27, s17, s22
	s_ashr_i32 s22, s66, 31
	s_mul_i32 s22, s48, s22
	s_mul_hi_u32 s23, s48, s66
	s_add_i32 s22, s23, s22
	s_mul_i32 s23, s47, s66
	s_add_i32 s49, s44, 0
	s_add_i32 s22, s22, s23
	s_mul_i32 s23, s48, s66
	s_add_i32 s50, s49, 0x2000
	s_add_u32 s28, s18, s23
	s_addc_u32 s29, s19, s22
	s_lshl_b32 s22, s65, 7
	s_add_i32 s22, s22, s31
	v_bfe_u32 v63, v0, 4, 2
	s_mul_i32 s34, s24, 48
	s_mov_b32 m0, s49
	v_or_b32_e32 v38, s22, v65
	s_mul_i32 s22, s66, 0xc0
	global_load_lds_dwordx4 v110, s[26:27]
	s_mov_b32 m0, s50
	s_add_i32 s51, s49, 0x4000
	s_add_i32 s22, s22, s34
	v_lshlrev_b32_e32 v66, 2, v63
	v_lshlrev_b32_e32 v112, 1, v4
	global_load_lds_dwordx4 v114, s[26:27]
	s_mov_b32 m0, s51
	s_add_i32 s52, s49, 0x6000
	v_or_b32_e32 v2, s22, v66
	v_mad_i64_i32 v[4:5], s[22:23], v38, s41, 0
	v_or_b32_e32 v12, 16, v38
	v_or_b32_e32 v26, 32, v38
	v_or_b32_e32 v38, 48, v38
	global_load_lds_dwordx4 v112, s[28:29]
	s_mov_b32 m0, s52
	s_add_i32 s53, s49, 0x8000
	v_ashrrev_i32_e32 v3, 31, v2
	v_mad_i64_i32 v[12:13], s[22:23], v12, s41, 0
	v_mad_i64_i32 v[26:27], s[22:23], v26, s41, 0
	v_mad_i64_i32 v[38:39], s[22:23], v38, s41, 0
	global_load_lds_dwordx4 v116, s[28:29]
	s_mov_b32 m0, s53
	v_lshl_add_u64 v[4:5], v[4:5], 2, s[8:9]
	v_lshlrev_b64 v[34:35], 2, v[2:3]
	v_lshl_add_u64 v[12:13], v[12:13], 2, s[8:9]
	v_lshl_add_u64 v[26:27], v[26:27], 2, s[8:9]
	v_lshl_add_u64 v[38:39], v[38:39], 2, s[8:9]
	global_load_lds_dwordx4 v118, s[28:29]
	v_lshl_add_u64 v[194:195], v[4:5], 0, v[34:35]
	v_lshl_add_u64 v[196:197], v[12:13], 0, v[34:35]
	v_lshl_add_u64 v[198:199], v[26:27], 0, v[34:35]
	v_lshl_add_u64 v[200:201], v[38:39], 0, v[34:35]
	s_load_dword s54, s[0:1], 0x58
	v_mov_b32_e32 v111, 0
	v_mov_b32_e32 v115, v111
	v_mov_b32_e32 v113, v111
	v_mov_b32_e32 v117, v111
	v_mov_b32_e32 v119, v111
	s_mov_b32 s55, 0
	s_cmp_lg_u32 s25, 1
	v_lshl_add_u64 v[60:61], s[26:27], 0, v[110:111]
	v_lshl_add_u64 v[58:59], s[26:27], 0, v[114:115]
	v_lshl_add_u64 v[56:57], s[28:29], 0, v[112:113]
	v_lshl_add_u64 v[54:55], s[28:29], 0, v[116:117]
	v_lshl_add_u64 v[52:53], s[28:29], 0, v[118:119]
	s_cbranch_scc1 .LBB4_8
	s_barrier

.LBB4_22:
	s_add_u32 s34, s26, s30
	s_addc_u32 s35, s27, s31
	s_add_u32 s34, s34, 0x180
	s_addc_u32 s35, s35, 0
	s_add_u32 s68, s28, s30
	s_addc_u32 s69, s29, s31
	s_add_u32 s70, s68, 0x180
	s_addc_u32 s71, s69, 0
	s_cmp_eq_u32 s60, s67
	s_cselect_b32 s69, s5, s35
	s_cselect_b32 s68, s4, s34
	s_cselect_b32 s35, s7, s71
	s_cselect_b32 s34, s6, s70
	s_add_i32 s70, s62, s44
	v_lshl_add_u64 v[108:109], v[98:99], 0, s[30:31]
	s_mov_b32 m0, s70
	ds_read_b128 v[130:133], v136 offset:16384
	ds_read_b128 v[142:145], v136 offset:17408
	ds_read_b128 v[146:149], v136 offset:18432
	ds_read_b128 v[150:153], v136 offset:19456
	ds_read_b128 v[154:157], v137
	ds_read_b128 v[158:161], v137 offset:1024
	ds_read_b128 v[162:165], v137 offset:2048
	ds_read_b128 v[166:169], v137 offset:3072
	ds_read_b128 v[170:173], v137 offset:4096
	ds_read_b128 v[174:177], v137 offset:5120
	ds_read_b128 v[178:181], v137 offset:6144
	ds_read_b128 v[182:185], v137 offset:7168
	global_load_lds_dwordx4 v[108:109], off
	v_lshl_add_u64 v[108:109], v[100:101], 0, s[30:31]
	s_add_i32 m0, s70, 0x2000
	s_nop 0
	global_load_lds_dwordx4 v[108:109], off
	s_barrier
	s_waitcnt lgkmcnt(0)
	s_setprio 1
	s_waitcnt lgkmcnt(0)
	v_mfma_f32_16x16x32_f16 v[94:97], v[130:133], v[154:157], v[94:97]
	v_mfma_f32_16x16x32_f16 v[90:93], v[146:149], v[154:157], v[90:93]
	v_mfma_f32_16x16x32_f16 v[82:85], v[130:133], v[162:165], v[82:85]
	v_mfma_f32_16x16x32_f16 v[78:81], v[146:149], v[162:165], v[78:81]
	v_mfma_f32_16x16x32_f16 v[70:73], v[130:133], v[170:173], v[70:73]
	v_mfma_f32_16x16x32_f16 v[66:69], v[146:149], v[170:173], v[66:69]
	v_mfma_f32_16x16x32_f16 v[58:61], v[130:133], v[178:181], v[58:61]
	v_mfma_f32_16x16x32_f16 v[54:57], v[146:149], v[178:181], v[54:57]
	v_mfma_f32_16x16x32_f16 v[94:97], v[142:145], v[158:161], v[94:97]
	v_mfma_f32_16x16x32_f16 v[90:93], v[150:153], v[158:161], v[90:93]
	v_mfma_f32_16x16x32_f16 v[82:85], v[142:145], v[166:169], v[82:85]
	v_mfma_f32_16x16x32_f16 v[78:81], v[150:153], v[166:169], v[78:81]
	v_mfma_f32_16x16x32_f16 v[70:73], v[142:145], v[174:177], v[70:73]
	v_mfma_f32_16x16x32_f16 v[66:69], v[150:153], v[174:177], v[66:69]
	v_mfma_f32_16x16x32_f16 v[58:61], v[142:145], v[182:185], v[58:61]
	v_mfma_f32_16x16x32_f16 v[54:57], v[150:153], v[182:185], v[54:57]
	s_setprio 0
	s_barrier
	v_lshl_add_u64 v[108:109], v[102:103], 0, s[30:31]
	s_add_i32 m0, s49, 0x18000
	ds_read_b128 v[130:133], v136 offset:20480
	ds_read_b128 v[142:145], v136 offset:21504
	global_load_lds_dwordx4 v[108:109], off
	v_lshl_add_u64 v[108:109], v[104:105], 0, s[30:31]
	s_add_i32 m0, s49, 0x1a000
	s_nop 0
	global_load_lds_dwordx4 v[108:109], off
	v_lshl_add_u64 v[108:109], v[106:107], 0, s[30:31]
	s_add_i32 m0, s49, 0x1c000
	s_nop 0
	global_load_lds_dwordx4 v[108:109], off
	s_cmp_lg_u32 s67, 0
	s_cbranch_scc1 .Lpj_norm_0
	global_load_dwordx4 v[2:5], v[194:195], off
	global_load_dwordx4 v[6:9], v[194:195], off offset:64
	global_load_dwordx4 v[10:13], v[194:195], off offset:128
	global_load_dwordx4 v[14:17], v[196:197], off
	s_waitcnt vmcnt(9)
	s_branch .Lpj_join_0
.Lpj_norm_0:
	s_waitcnt vmcnt(5)
.Lpj_join_0:
	s_barrier
	s_waitcnt lgkmcnt(0)
	s_setprio 1
	s_waitcnt lgkmcnt(0)
	v_mfma_f32_16x16x32_f16 v[86:89], v[130:133], v[154:157], v[86:89]
	v_mfma_f32_16x16x32_f16 v[74:77], v[130:133], v[162:165], v[74:77]
	v_mfma_f32_16x16x32_f16 v[62:65], v[130:133], v[170:173], v[62:65]
	v_mfma_f32_16x16x32_f16 v[50:53], v[130:133], v[178:181], v[50:53]
	v_mfma_f32_16x16x32_f16 v[86:89], v[142:145], v[158:161], v[86:89]
	v_mfma_f32_16x16x32_f16 v[74:77], v[142:145], v[166:169], v[74:77]
	v_mfma_f32_16x16x32_f16 v[62:65], v[142:145], v[174:177], v[62:65]
	v_mfma_f32_16x16x32_f16 v[50:53], v[142:145], v[182:185], v[50:53]
	s_setprio 0
	s_barrier
	s_mov_b32 m0, s49
	v_lshl_add_u64 v[108:109], s[68:69], 0, v[110:111]
	ds_read_b128 v[130:133], v136 offset:57344
	ds_read_b128 v[142:145], v136 offset:58368
	ds_read_b128 v[146:149], v136 offset:59392
	ds_read_b128 v[150:153], v136 offset:60416
	ds_read_b128 v[154:157], v137 offset:40960
	ds_read_b128 v[158:161], v137 offset:41984
	ds_read_b128 v[162:165], v137 offset:43008
	ds_read_b128 v[166:169], v137 offset:44032
	ds_read_b128 v[170:173], v137 offset:45056
	ds_read_b128 v[174:177], v137 offset:46080
	ds_read_b128 v[178:181], v137 offset:47104
	ds_read_b128 v[182:185], v137 offset:48128
	global_load_lds_dwordx4 v[108:109], off
	v_lshl_add_u64 v[186:187], s[68:69], 0, v[114:115]
	s_mov_b32 m0, s50
	s_nop 0
	global_load_lds_dwordx4 v[186:187], off
	s_barrier
	s_waitcnt lgkmcnt(0)
	s_setprio 1
	s_waitcnt lgkmcnt(0)
	v_mfma_f32_16x16x32_f16 v[94:97], v[130:133], v[154:157], v[94:97]
	v_mfma_f32_16x16x32_f16 v[90:93], v[146:149], v[154:157], v[90:93]
	v_mfma_f32_16x16x32_f16 v[82:85], v[130:133], v[162:165], v[82:85]
	v_mfma_f32_16x16x32_f16 v[78:81], v[146:149], v[162:165], v[78:81]
	v_mfma_f32_16x16x32_f16 v[70:73], v[130:133], v[170:173], v[70:73]
	v_mfma_f32_16x16x32_f16 v[66:69], v[146:149], v[170:173], v[66:69]
	v_mfma_f32_16x16x32_f16 v[58:61], v[130:133], v[178:181], v[58:61]
	v_mfma_f32_16x16x32_f16 v[54:57], v[146:149], v[178:181], v[54:57]
	v_mfma_f32_16x16x32_f16 v[94:97], v[142:145], v[158:161], v[94:97]
	v_mfma_f32_16x16x32_f16 v[90:93], v[150:153], v[158:161], v[90:93]
	v_mfma_f32_16x16x32_f16 v[82:85], v[142:145], v[166:169], v[82:85]
	v_mfma_f32_16x16x32_f16 v[78:81], v[150:153], v[166:169], v[78:81]
	v_mfma_f32_16x16x32_f16 v[70:73], v[142:145], v[174:177], v[70:73]
	v_mfma_f32_16x16x32_f16 v[66:69], v[150:153], v[174:177], v[66:69]
	v_mfma_f32_16x16x32_f16 v[58:61], v[142:145], v[182:185], v[58:61]
	v_mfma_f32_16x16x32_f16 v[54:57], v[150:153], v[182:185], v[54:57]
	s_setprio 0
	s_barrier
	s_mov_b32 m0, s51
	v_lshl_add_u64 v[188:189], s[34:35], 0, v[112:113]
	ds_read_b128 v[130:133], v136 offset:61440
	ds_read_b128 v[142:145], v136 offset:62464
	global_load_lds_dwordx4 v[188:189], off
	v_lshl_add_u64 v[190:191], s[34:35], 0, v[116:117]
	s_mov_b32 m0, s52
	v_lshl_add_u64 v[192:193], s[34:35], 0, v[118:119]
	global_load_lds_dwordx4 v[190:191], off
	s_mov_b32 m0, s53
	s_nop 0
	global_load_lds_dwordx4 v[192:193], off
	s_cmp_lg_u32 s67, 0
	s_cbranch_scc1 .Lpj_norm_1
	global_load_dwordx4 v[18:21], v[196:197], off offset:64
	global_load_dwordx4 v[22:25], v[196:197], off offset:128
	global_load_dwordx4 v[26:29], v[198:199], off
	global_load_dwordx4 v[30:33], v[198:199], off offset:64
	s_waitcnt vmcnt(13)
	s_branch .Lpj_join_1

.Lpj_join_1:
	s_barrier
	s_waitcnt lgkmcnt(0)
	s_setprio 1
	s_waitcnt lgkmcnt(0)
	v_mfma_f32_16x16x32_f16 v[86:89], v[130:133], v[154:157], v[86:89]
	v_mfma_f32_16x16x32_f16 v[74:77], v[130:133], v[162:165], v[74:77]
	v_mfma_f32_16x16x32_f16 v[62:65], v[130:133], v[170:173], v[62:65]
	v_mfma_f32_16x16x32_f16 v[50:53], v[130:133], v[178:181], v[50:53]
	v_mfma_f32_16x16x32_f16 v[86:89], v[142:145], v[158:161], v[86:89]
	v_mfma_f32_16x16x32_f16 v[74:77], v[142:145], v[166:169], v[74:77]
	v_mfma_f32_16x16x32_f16 v[62:65], v[142:145], v[174:177], v[62:65]
	v_mfma_f32_16x16x32_f16 v[50:53], v[142:145], v[182:185], v[50:53]
	s_setprio 0
	s_barrier
	s_mov_b32 m0, s56
	v_lshl_add_u64 v[108:109], v[108:109], 0, s[22:23]
	ds_read_b128 v[130:133], v138
	ds_read_b128 v[142:145], v138 offset:1024
	ds_read_b128 v[146:149], v138 offset:2048
	ds_read_b128 v[150:153], v138 offset:3072
	ds_read_b128 v[154:157], v139
	ds_read_b128 v[158:161], v139 offset:1024
	ds_read_b128 v[162:165], v139 offset:2048
	ds_read_b128 v[166:169], v139 offset:3072
	ds_read_b128 v[170:173], v139 offset:4096
	ds_read_b128 v[174:177], v139 offset:5120
	ds_read_b128 v[178:181], v139 offset:6144
	ds_read_b128 v[182:185], v139 offset:7168
	global_load_lds_dwordx4 v[108:109], off
	v_lshl_add_u64 v[108:109], v[186:187], 0, s[22:23]
	s_mov_b32 m0, s57
	s_nop 0
	global_load_lds_dwordx4 v[108:109], off
	s_barrier
	s_waitcnt lgkmcnt(0)
	s_setprio 1
	s_waitcnt lgkmcnt(0)
	v_mfma_f32_16x16x32_f16 v[94:97], v[130:133], v[154:157], v[94:97]
	v_mfma_f32_16x16x32_f16 v[90:93], v[146:149], v[154:157], v[90:93]
	v_mfma_f32_16x16x32_f16 v[82:85], v[130:133], v[162:165], v[82:85]
	v_mfma_f32_16x16x32_f16 v[78:81], v[146:149], v[162:165], v[78:81]
	v_mfma_f32_16x16x32_f16 v[70:73], v[130:133], v[170:173], v[70:73]
	v_mfma_f32_16x16x32_f16 v[66:69], v[146:149], v[170:173], v[66:69]
	v_mfma_f32_16x16x32_f16 v[58:61], v[130:133], v[178:181], v[58:61]
	v_mfma_f32_16x16x32_f16 v[54:57], v[146:149], v[178:181], v[54:57]
	v_mfma_f32_16x16x32_f16 v[94:97], v[142:145], v[158:161], v[94:97]
	v_mfma_f32_16x16x32_f16 v[90:93], v[150:153], v[158:161], v[90:93]
	v_mfma_f32_16x16x32_f16 v[82:85], v[142:145], v[166:169], v[82:85]
	v_mfma_f32_16x16x32_f16 v[78:81], v[150:153], v[166:169], v[78:81]
	v_mfma_f32_16x16x32_f16 v[70:73], v[142:145], v[174:177], v[70:73]
	v_mfma_f32_16x16x32_f16 v[66:69], v[150:153], v[174:177], v[66:69]
	v_mfma_f32_16x16x32_f16 v[58:61], v[142:145], v[182:185], v[58:61]
	v_mfma_f32_16x16x32_f16 v[54:57], v[150:153], v[182:185], v[54:57]
	s_setprio 0
	s_barrier
	s_mov_b32 m0, s58
	v_lshl_add_u64 v[108:109], v[188:189], 0, s[22:23]
	ds_read_b128 v[130:133], v138 offset:4096
	ds_read_b128 v[142:145], v138 offset:5120
	global_load_lds_dwordx4 v[108:109], off
	v_lshl_add_u64 v[108:109], v[190:191], 0, s[22:23]
	s_add_i32 m0, s58, 0x2000
	s_nop 0
	global_load_lds_dwordx4 v[108:109], off
	v_lshl_add_u64 v[108:109], v[192:193], 0, s[22:23]
	s_add_i32 m0, s58, 0x4000
	s_nop 0
	global_load_lds_dwordx4 v[108:109], off
	s_cmp_lg_u32 s67, 0
	s_cbranch_scc1 .Lpj_norm_2
	global_load_dwordx4 v[34:37], v[198:199], off offset:128
	global_load_dwordx4 v[38:41], v[200:201], off
	global_load_dwordx4 v[42:45], v[200:201], off offset:64
	global_load_dwordx4 v[46:49], v[200:201], off offset:128
	s_waitcnt vmcnt(13)
	s_branch .Lpj_join_2

.Lpj_join_2:
	s_barrier
	s_waitcnt lgkmcnt(0)
	s_setprio 1
	s_waitcnt lgkmcnt(0)
	v_mfma_f32_16x16x32_f16 v[86:89], v[130:133], v[154:157], v[86:89]
	v_mfma_f32_16x16x32_f16 v[74:77], v[130:133], v[162:165], v[74:77]
	v_mfma_f32_16x16x32_f16 v[62:65], v[130:133], v[170:173], v[62:65]
	v_mfma_f32_16x16x32_f16 v[50:53], v[130:133], v[178:181], v[50:53]
	v_mfma_f32_16x16x32_f16 v[86:89], v[142:145], v[158:161], v[86:89]
	v_mfma_f32_16x16x32_f16 v[74:77], v[142:145], v[166:169], v[74:77]
	v_mfma_f32_16x16x32_f16 v[62:65], v[142:145], v[174:177], v[62:65]
	v_mfma_f32_16x16x32_f16 v[50:53], v[142:145], v[182:185], v[50:53]
	s_setprio 0
	s_barrier
	s_add_i32 s67, s67, 3
	s_add_u32 s30, s30, 0x180
	s_addc_u32 s31, s31, 0
	s_cmp_ge_i32 s67, s59
	s_cbranch_scc0 .LBB4_22

	.amdhsa_kernel _Z9k_gemm192IN4g19210EpiResStatEEvNS0_4GemmET_
		.amdhsa_group_segment_fixed_size 0
		.amdhsa_private_segment_fixed_size 0
		.amdhsa_kernarg_size 344
		.amdhsa_user_sgpr_count 2
		.amdhsa_user_sgpr_dispatch_ptr 0
		.amdhsa_user_sgpr_queue_ptr 0
		.amdhsa_user_sgpr_kernarg_segment_ptr 1
		.amdhsa_user_sgpr_dispatch_id 0
		.amdhsa_user_sgpr_kernarg_preload_length 0
		.amdhsa_user_sgpr_kernarg_preload_offset 0
		.amdhsa_user_sgpr_private_segment_size 0
		.amdhsa_uses_dynamic_stack 0
		.amdhsa_enable_private_segment 0
		.amdhsa_system_sgpr_workgroup_id_x 1
		.amdhsa_system_sgpr_workgroup_id_y 0
		.amdhsa_system_sgpr_workgroup_id_z 0
		.amdhsa_system_sgpr_workgroup_info 0
		.amdhsa_system_vgpr_workitem_id 0
		.amdhsa_next_free_vgpr 202
		.amdhsa_next_free_sgpr 72
		.amdhsa_accum_offset 204
		.amdhsa_reserve_vcc 1
		.amdhsa_float_round_mode_32 0
		.amdhsa_float_round_mode_16_64 0
		.amdhsa_float_denorm_mode_32 3
		.amdhsa_float_denorm_mode_16_64 3
		.amdhsa_dx10_clamp 1
		.amdhsa_ieee_mode 1
		.amdhsa_fp16_overflow 0
		.amdhsa_tg_split 0
		.amdhsa_exception_fp_ieee_invalid_op 0
		.amdhsa_exception_fp_denorm_src 0
		.amdhsa_exception_fp_ieee_div_zero 0
		.amdhsa_exception_fp_ieee_overflow 0
		.amdhsa_exception_fp_ieee_underflow 0
		.amdhsa_exception_fp_ieee_inexact 0
		.amdhsa_exception_int_div_zero 0
	.end_amdhsa_kernel

	.text
	.p2alignl 6, 3212836864
	.fill 256, 4, 3212836864
	.p2alignl 8, 3212836864

amdhsa.kernels:
  - .agpr_count:     0
    .args:
      - .offset:         0
        .size:           224
        .value_kind:     by_value
      - .actual_access:  read_only
        .address_space:  global
        .offset:         224
        .size:           8
        .value_kind:     global_buffer
      - .actual_access:  read_only
        .address_space:  global
        .offset:         232
        .size:           8
        .value_kind:     global_buffer
      - .actual_access:  read_only
        .address_space:  global
        .offset:         240
        .size:           8
        .value_kind:     global_buffer
      - .actual_access:  write_only
        .address_space:  global
        .offset:         248
        .size:           8
        .value_kind:     global_buffer
      - .offset:         256
        .size:           4
        .value_kind:     hidden_block_count_x
      - .offset:         260
        .size:           4
        .value_kind:     hidden_block_count_y
      - .offset:         264
        .size:           4
        .value_kind:     hidden_block_count_z
      - .offset:         268
        .size:           2
        .value_kind:     hidden_group_size_x
      - .offset:         270
        .size:           2
        .value_kind:     hidden_group_size_y
      - .offset:         272
        .size:           2
        .value_kind:     hidden_group_size_z
      - .offset:         274
        .size:           2
        .value_kind:     hidden_remainder_x
      - .offset:         276
        .size:           2
        .value_kind:     hidden_remainder_y
      - .offset:         278
        .size:           2
        .value_kind:     hidden_remainder_z
      - .offset:         296
        .size:           8
        .value_kind:     hidden_global_offset_x
      - .offset:         304
        .size:           8
        .value_kind:     hidden_global_offset_y
      - .offset:         312
        .size:           8
        .value_kind:     hidden_global_offset_z
      - .offset:         320
        .size:           2
        .value_kind:     hidden_grid_dims
    .group_segment_fixed_size: 16640
    .kernarg_segment_align: 8
    .kernarg_segment_size: 512
    .language:       OpenCL C
    .language_version:
      - 2
      - 0
    .max_flat_workgroup_size: 256
    .name:           _Z10k_prep_ln18PrepArgsPKfS1_S1_Pt
    .private_segment_fixed_size: 0
    .sgpr_count:     28
    .sgpr_spill_count: 0
    .symbol:         _Z10k_prep_ln18PrepArgsPKfS1_S1_Pt.kd
    .uniform_work_group_size: 1
    .uses_dynamic_stack: false
    .vgpr_count:     75
    .vgpr_spill_count: 0
    .wavefront_size: 64
  - .agpr_count:     0
    .args:
      - .actual_access:  read_only
        .address_space:  global
        .offset:         0
        .size:           8
        .value_kind:     global_buffer
      - .actual_access:  read_only
        .address_space:  global
        .offset:         8
        .size:           8
        .value_kind:     global_buffer
      - .actual_access:  read_only
        .address_space:  global
        .offset:         16
        .size:           8
        .value_kind:     global_buffer
      - .actual_access:  write_only
        .address_space:  global
        .offset:         24
        .size:           8
        .value_kind:     global_buffer
    .group_segment_fixed_size: 0
    .kernarg_segment_align: 8
    .kernarg_segment_size: 32
    .language:       OpenCL C
    .language_version:
      - 2
      - 0
    .max_flat_workgroup_size: 256
    .name:           _Z5k_ln2PKfS0_S0_Pt
    .private_segment_fixed_size: 0
    .sgpr_count:     18
    .sgpr_spill_count: 0
    .symbol:         _Z5k_ln2PKfS0_S0_Pt.kd
    .uniform_work_group_size: 1
    .uses_dynamic_stack: false
    .vgpr_count:     54
    .vgpr_spill_count: 0
    .wavefront_size: 64
  - .agpr_count:     0
    .args:
      - .actual_access:  read_only
        .address_space:  global
        .offset:         0
        .size:           8
        .value_kind:     global_buffer
      - .actual_access:  read_only
        .address_space:  global
        .offset:         8
        .size:           8
        .value_kind:     global_buffer
      - .actual_access:  read_only
        .address_space:  global
        .offset:         16
        .size:           8
        .value_kind:     global_buffer
      - .actual_access:  read_only
        .address_space:  global
        .offset:         24
        .size:           8
        .value_kind:     global_buffer
      - .actual_access:  read_only
        .address_space:  global
        .offset:         32
        .size:           8
        .value_kind:     global_buffer
      - .actual_access:  write_only
        .address_space:  global
        .offset:         40
        .size:           8
        .value_kind:     global_buffer
      - .offset:         48
        .size:           224
        .value_kind:     by_value
    .group_segment_fixed_size: 0
    .kernarg_segment_align: 8
    .kernarg_segment_size: 272
    .language:       OpenCL C
    .language_version:
      - 2
      - 0
    .max_flat_workgroup_size: 256
    .name:           _Z6k_attnPKtS0_S0_S0_S0_Pt8PrepArgs
    .private_segment_fixed_size: 0
    .sgpr_count:     30
    .sgpr_spill_count: 0
    .symbol:         _Z6k_attnPKtS0_S0_S0_S0_Pt8PrepArgs.kd
    .uniform_work_group_size: 1
    .uses_dynamic_stack: false
    .vgpr_count:     244
    .vgpr_spill_count: 0
    .wavefront_size: 64
  - .agpr_count:     0
    .args:
      - .offset:         0
        .size:           40
        .value_kind:     by_value
      - .offset:         40
        .size:           32
        .value_kind:     by_value
      - .offset:         72
        .size:           4
        .value_kind:     hidden_block_count_x
      - .offset:         76
        .size:           4
        .value_kind:     hidden_block_count_y
      - .offset:         80
        .size:           4
        .value_kind:     hidden_block_count_z
      - .offset:         84
        .size:           2
        .value_kind:     hidden_group_size_x
      - .offset:         86
        .size:           2
        .value_kind:     hidden_group_size_y
      - .offset:         88
        .size:           2
        .value_kind:     hidden_group_size_z
      - .offset:         90
        .size:           2
        .value_kind:     hidden_remainder_x
      - .offset:         92
        .size:           2
        .value_kind:     hidden_remainder_y
      - .offset:         94
        .size:           2
        .value_kind:     hidden_remainder_z
      - .offset:         112
        .size:           8
        .value_kind:     hidden_global_offset_x
      - .offset:         120
        .size:           8
        .value_kind:     hidden_global_offset_y
      - .offset:         128
        .size:           8
        .value_kind:     hidden_global_offset_z
      - .offset:         136
        .size:           2
        .value_kind:     hidden_grid_dims
      - .offset:         192
        .size:           4
        .value_kind:     hidden_dynamic_lds_size
    .group_segment_fixed_size: 0
    .kernarg_segment_align: 8
    .kernarg_segment_size: 328
    .language:       OpenCL C
    .language_version:
      - 2
      - 0
    .max_flat_workgroup_size: 512
    .name:           _Z9k_gemm192IN4g1926EpiQKVEEvNS0_4GemmET_
    .private_segment_fixed_size: 0
    .sgpr_count:     74
    .sgpr_spill_count: 0
    .symbol:         _Z9k_gemm192IN4g1926EpiQKVEEvNS0_4GemmET_.kd
    .uniform_work_group_size: 1
    .uses_dynamic_stack: false
    .vgpr_count:     156
    .vgpr_spill_count: 0
    .wavefront_size: 64
  - .agpr_count:     0
    .args:
      - .offset:         0
        .size:           40
        .value_kind:     by_value
      - .offset:         40
        .size:           48
        .value_kind:     by_value
      - .offset:         88
        .size:           4
        .value_kind:     hidden_block_count_x
      - .offset:         92
        .size:           4
        .value_kind:     hidden_block_count_y
      - .offset:         96
        .size:           4
        .value_kind:     hidden_block_count_z
      - .offset:         100
        .size:           2
        .value_kind:     hidden_group_size_x
      - .offset:         102
        .size:           2
        .value_kind:     hidden_group_size_y
      - .offset:         104
        .size:           2
        .value_kind:     hidden_group_size_z
      - .offset:         106
        .size:           2
        .value_kind:     hidden_remainder_x
      - .offset:         108
        .size:           2
        .value_kind:     hidden_remainder_y
      - .offset:         110
        .size:           2
        .value_kind:     hidden_remainder_z
      - .offset:         128
        .size:           8
        .value_kind:     hidden_global_offset_x
      - .offset:         136
        .size:           8
        .value_kind:     hidden_global_offset_y
      - .offset:         144
        .size:           8
        .value_kind:     hidden_global_offset_z
      - .offset:         152
        .size:           2
        .value_kind:     hidden_grid_dims
      - .offset:         208
        .size:           4
        .value_kind:     hidden_dynamic_lds_size
    .group_segment_fixed_size: 0
    .kernarg_segment_align: 8
    .kernarg_segment_size: 344
    .language:       OpenCL C
    .language_version:
      - 2
      - 0
    .max_flat_workgroup_size: 512
    .name:           _Z9k_gemm192IN4g19210EpiResStatEEvNS0_4GemmET_
    .private_segment_fixed_size: 0
    .sgpr_count:     78
    .sgpr_spill_count: 0
    .symbol:         _Z9k_gemm192IN4g19210EpiResStatEEvNS0_4GemmET_.kd
    .uniform_work_group_size: 1
    .uses_dynamic_stack: false
    .vgpr_count:     202
    .vgpr_spill_count: 0
    .wavefront_size: 64
  - .agpr_count:     0
    .args:
      - .offset:         0
        .size:           40
        .value_kind:     by_value
      - .offset:         40
        .size:           48
        .value_kind:     by_value
      - .offset:         88
        .size:           4
        .value_kind:     hidden_block_count_x
      - .offset:         92
        .size:           4
        .value_kind:     hidden_block_count_y
      - .offset:         96
        .size:           4
        .value_kind:     hidden_block_count_z
      - .offset:         100
        .size:           2
        .value_kind:     hidden_group_size_x
      - .offset:         102
        .size:           2
        .value_kind:     hidden_group_size_y
      - .offset:         104
        .size:           2
        .value_kind:     hidden_group_size_z
      - .offset:         106
        .size:           2
        .value_kind:     hidden_remainder_x
      - .offset:         108
        .size:           2
        .value_kind:     hidden_remainder_y
      - .offset:         110
        .size:           2
        .value_kind:     hidden_remainder_z
      - .offset:         128
        .size:           8
        .value_kind:     hidden_global_offset_x
      - .offset:         136
        .size:           8
        .value_kind:     hidden_global_offset_y
      - .offset:         144
        .size:           8
        .value_kind:     hidden_global_offset_z
      - .offset:         152
        .size:           2
        .value_kind:     hidden_grid_dims
      - .offset:         208
        .size:           4
        .value_kind:     hidden_dynamic_lds_size
    .group_segment_fixed_size: 0
    .kernarg_segment_align: 8
    .kernarg_segment_size: 344
    .language:       OpenCL C
    .language_version:
      - 2
      - 0
    .max_flat_workgroup_size: 512
    .name:           _Z9k_gemm128IN4g1289EpiGeluLNEEvNS0_4GemmET_
    .private_segment_fixed_size: 0
    .sgpr_count:     84
    .sgpr_spill_count: 0
    .symbol:         _Z9k_gemm128IN4g1289EpiGeluLNEEvNS0_4GemmET_.kd
    .uniform_work_group_size: 1
    .uses_dynamic_stack: false
    .vgpr_count:     170
    .vgpr_spill_count: 0
    .wavefront_size: 64
  - .agpr_count:     0
    .args:
      - .offset:         0
        .size:           40
        .value_kind:     by_value
      - .offset:         40
        .size:           32
        .value_kind:     by_value
      - .offset:         72
        .size:           4
        .value_kind:     hidden_block_count_x
      - .offset:         76
        .size:           4
        .value_kind:     hidden_block_count_y
      - .offset:         80
        .size:           4
        .value_kind:     hidden_block_count_z
      - .offset:         84
        .size:           2
        .value_kind:     hidden_group_size_x
      - .offset:         86
        .size:           2
        .value_kind:     hidden_group_size_y
      - .offset:         88
        .size:           2
        .value_kind:     hidden_group_size_z
      - .offset:         90
        .size:           2
        .value_kind:     hidden_remainder_x
      - .offset:         92
        .size:           2
        .value_kind:     hidden_remainder_y
      - .offset:         94
        .size:           2
        .value_kind:     hidden_remainder_z
      - .offset:         112
        .size:           8
        .value_kind:     hidden_global_offset_x
      - .offset:         120
        .size:           8
        .value_kind:     hidden_global_offset_y
      - .offset:         128
        .size:           8
        .value_kind:     hidden_global_offset_z
      - .offset:         136
        .size:           2
        .value_kind:     hidden_grid_dims
      - .offset:         192
        .size:           4
        .value_kind:     hidden_dynamic_lds_size
    .group_segment_fixed_size: 0
    .kernarg_segment_align: 8
    .kernarg_segment_size: 328
    .language:       OpenCL C
    .language_version:
      - 2
      - 0
    .max_flat_workgroup_size: 512
    .name:           _Z9k_gemm192IN4g1927EpiResHEEvNS0_4GemmET_
    .private_segment_fixed_size: 0
    .sgpr_count:     76
    .sgpr_spill_count: 0
    .symbol:         _Z9k_gemm192IN4g1927EpiResHEEvNS0_4GemmET_.kd
    .uniform_work_group_size: 1
    .uses_dynamic_stack: false
    .vgpr_count:     190
    .vgpr_spill_count: 0
    .wavefront_size: 64
